# phase 3: the cumulative-sum items' four strided forget-gate loads are issued at the start of the phase into v251..v254 by the workgroups that run an item (grid 256), on top of the combined version
# speedup vs baseline: 1.0096x; 1.0007x over previous
.LBB0_469:
	s_cmp_lt_i32 s78, 4
	v_writelane_b32 v255, s84, 0
	s_cselect_b64 s[6:7], -1, 0
	s_nop 0
	v_writelane_b32 v255, s85, 1
	s_and_b64 s[84:85], s[6:7], s[4:5]
	s_andn2_b64 vcc, exec, s[84:85]
	s_cbranch_vccnz .LBB0_571
	s_cmp_eq_u32 s80, 0x100
	s_cbranch_scc0 .Lp3c_nopf
	s_cmp_lt_u32 s2, 32
	s_cbranch_scc0 .Lp3c_nopf
	s_and_b32 s98, s2, 7
	s_lshr_b32 s99, s98, 1
	s_lshl_b32 s99, s99, 3
	s_and_b32 s98, s98, 1
	s_lshl_b32 s98, s98, 2
	s_add_u32 s99, s99, s98
	s_lshr_b32 s98, s2, 3
	s_add_u32 s100, s99, s98
	s_lshr_b32 s98, s100, 3
	s_lshl_b32 s98, s98, 21
	s_and_b32 s99, s100, 7
	s_lshl_b32 s99, s99, 2
	s_add_u32 s98, s98, s99
	s_add_u32 s98, s98, 0x20338140
	s_add_u32 s98, s76, s98
	s_addc_u32 s99, s77, 0
	v_lshlrev_b32_e32 v254, 12, v250
	global_load_dword v251, v254, s[98:99]
	global_load_dword v252, v254, s[98:99] offset:1024
	global_load_dword v253, v254, s[98:99] offset:2048
	global_load_dword v254, v254, s[98:99] offset:3072
.Lp3c_nopf:
	s_cmpk_lt_i32 s2, 0x100
	v_writelane_b32 v255, s82, 2
	s_cselect_b64 s[4:5], -1, 0
	v_and_b32_e32 v217, 63, v250
	v_writelane_b32 v255, s4, 3
	v_lshrrev_b32_e32 v1, 6, v250
	s_cmpk_gt_i32 s2, 0xff
	v_writelane_b32 v255, s5, 4
	v_lshlrev_b32_e32 v216, 2, v250
	v_cmp_gt_u32_e64 s[4:5], 32, v217
	v_cmp_eq_u32_e64 s[6:7], 0, v217
	s_cbranch_scc1 .LBB0_550
	v_and_b32_e32 v162, 48, v250
	v_mov_b32_e32 v163, 0
	v_lshl_add_u64 v[2:3], s[76:77], 0, v[162:163]
	s_mov_b64 s[8:9], 0x1f338000
	v_lshl_add_u64 v[164:165], v[2:3], 0, s[8:9]
	s_mov_b64 s[8:9], 0x38218000
	s_movk_i32 s3, 0x4020
	v_lshl_add_u64 v[166:167], v[2:3], 0, s[8:9]
	v_mad_u32_u24 v2, v1, s3, 0
	v_or_b32_e32 v0, 0xf00, v216
	v_or_b32_e32 v3, 0x1f00, v216
	v_lshl_add_u32 v218, v217, 2, v2
	v_add_u32_e32 v219, v2, v0
	v_add_u32_e32 v220, v2, v3
	v_lshlrev_b32_e32 v2, 3, v217
	v_mov_b32_e32 v3, v163
	v_lshl_add_u64 v[2:3], s[76:77], 0, v[2:3]
	s_mov_b64 s[72:73], 0x29b38000
	v_and_b32_e32 v169, 15, v250
	v_lshl_add_u64 v[170:171], v[2:3], 0, s[72:73]
	v_lshlrev_b32_e32 v2, 6, v1
	s_movk_i32 s3, 0x2010
	v_lshlrev_b32_e32 v0, 10, v1
	v_mad_u32_u24 v2, v169, s3, v2
	v_lshlrev_b32_e32 v168, 1, v1
	s_mov_b32 s89, 0
	v_cmp_eq_u32_e64 s[8:9], 1, v217
	v_cmp_eq_u32_e64 s[10:11], 2, v217
	v_cmp_eq_u32_e64 s[12:13], 3, v217
	v_cmp_eq_u32_e64 s[14:15], 4, v217
	v_cmp_eq_u32_e64 s[16:17], 5, v217
	v_cmp_eq_u32_e64 s[18:19], 6, v217
	v_cmp_eq_u32_e64 s[20:21], 7, v217
	v_cmp_eq_u32_e64 s[22:23], 8, v217
	v_cmp_eq_u32_e64 s[24:25], 9, v217
	v_cmp_eq_u32_e64 s[26:27], 10, v217
	v_cmp_eq_u32_e64 s[28:29], 11, v217
	v_cmp_eq_u32_e64 s[30:31], 12, v217
	v_cmp_eq_u32_e64 s[34:35], 13, v217
	v_cmp_eq_u32_e64 s[36:37], 14, v217
	v_cmp_eq_u32_e64 s[38:39], 15, v217
	v_cmp_eq_u32_e64 s[40:41], 16, v217
	v_cmp_eq_u32_e64 s[42:43], 17, v217
	v_cmp_eq_u32_e64 s[44:45], 18, v217
	v_cmp_eq_u32_e64 s[46:47], 19, v217
	v_cmp_eq_u32_e64 s[48:49], 20, v217
	v_cmp_eq_u32_e64 s[50:51], 21, v217
	v_cmp_eq_u32_e64 s[52:53], 22, v217
	v_cmp_eq_u32_e64 s[54:55], 23, v217
	v_cmp_eq_u32_e64 s[56:57], 24, v217
	v_cmp_eq_u32_e64 s[58:59], 25, v217
	v_cmp_eq_u32_e64 s[60:61], 26, v217
	v_cmp_eq_u32_e64 s[62:63], 27, v217
	v_cmp_eq_u32_e64 s[64:65], 28, v217
	v_cmp_eq_u32_e64 s[66:67], 29, v217
	v_cmp_eq_u32_e64 s[68:69], 30, v217
	v_cmp_eq_u32_e64 s[70:71], 31, v217
	v_add3_u32 v221, v2, v162, 0
	s_mov_b64 s[90:91], 0x20338100
	s_mov_b32 s3, 0x20338000
	v_lshlrev_b32_e32 v172, 1, v0
	v_mov_b32_e32 v173, v163
	s_mov_b32 s81, s2
	s_branch .LBB0_473

.LBB0_560:
	s_lshl_b32 s31, s30, 8
	s_and_b32 s31, s31, 0xfffff800
	s_and_b32 s24, s30, 7
	v_or_b32_e32 v4, s31, v216
	v_ashrrev_i32_e32 v5, 31, v4
	s_lshl_b32 s24, s24, 2
	v_lshlrev_b64 v[4:5], 10, v[4:5]
	v_mov_b32_e32 v8, s24
	v_lshl_add_u64 v[4:5], s[76:77], 0, v[4:5]
	s_waitcnt lgkmcnt(0)
	global_load_dword v8, v8, s[26:27]
	v_lshl_add_u64 v[6:7], v[4:5], 0, s[24:25]
	v_lshl_add_u64 v[4:5], v[6:7], 0, s[28:29]
	v_add_co_u32_e32 v6, vcc, 0x20338000, v6
	s_nop 1
	v_addc_co_u32_e32 v7, vcc, 0, v7, vcc
	s_cmp_eq_u32 s80, 0x100
	s_cbranch_scc1 .Lp3c_usepf
	global_load_dword v19, v[4:5], off offset:1024
	global_load_dword v20, v[6:7], off offset:320
	global_load_dword v21, v[4:5], off offset:2048
	global_load_dword v22, v[4:5], off offset:3072
	s_branch .Lp3c_join
.Lp3c_usepf:
	s_waitcnt vmcnt(0)
	v_mov_b32_e32 v20, v251
	v_mov_b32_e32 v19, v252
	v_mov_b32_e32 v21, v253
	v_mov_b32_e32 v22, v254
.Lp3c_join:
	s_barrier
	s_waitcnt vmcnt(3)
	v_add_f32_e32 v4, v8, v19
	v_mul_f32_e64 v6, |v4|, s3
	s_waitcnt vmcnt(2)
	v_add_f32_e32 v5, v8, v20
	v_exp_f32_e32 v19, v6
	v_mul_f32_e64 v7, |v5|, s3
	v_exp_f32_e32 v20, v7
	v_min_f32_e32 v23, 0, v4
	v_add_f32_e32 v25, 1.0, v19
	v_min_f32_e32 v24, 0, v5
	v_frexp_mant_f32_e32 v28, v25
	v_cvt_f64_f32_e32 v[4:5], v25
	v_add_f32_e32 v26, 1.0, v20
	v_frexp_exp_i32_f64_e32 v4, v[4:5]
	v_cmp_gt_f32_e32 vcc, s40, v28
	v_add_f32_e32 v27, -1.0, v25
	v_add_f32_e32 v29, -1.0, v26
	v_frexp_mant_f32_e32 v30, v26
	v_cvt_f64_f32_e32 v[6:7], v26
	v_subbrev_co_u32_e32 v28, vcc, 0, v4, vcc
	v_sub_f32_e32 v31, v27, v25
	v_sub_f32_e32 v5, v29, v26
	v_frexp_exp_i32_f64_e32 v6, v[6:7]
	v_cmp_gt_f32_e32 vcc, s40, v30
	v_sub_f32_e32 v27, v19, v27
	v_add_f32_e32 v7, 1.0, v31
	v_add_f32_e32 v4, 1.0, v5
	v_subbrev_co_u32_e32 v5, vcc, 0, v6, vcc
	v_sub_f32_e32 v29, v20, v29
	v_add_f32_e32 v6, v27, v7
	v_sub_u32_e32 v7, 0, v28
	v_sub_u32_e32 v27, 0, v5
	v_add_f32_e32 v4, v29, v4
	v_cvt_f32_i32_e32 v5, v5
	v_ldexp_f32 v25, v25, v7
	v_ldexp_f32 v6, v6, v7
	v_ldexp_f32 v7, v26, v27
	v_ldexp_f32 v4, v4, v27
	v_add_f32_e32 v27, -1.0, v7
	v_add_f32_e32 v29, 1.0, v7
	v_add_f32_e32 v31, 1.0, v27
	v_add_f32_e32 v32, -1.0, v29
	v_sub_f32_e32 v31, v7, v31
	v_sub_f32_e32 v7, v7, v32
	v_mul_f32_e32 v32, 0x3f317218, v5
	v_add_f32_e32 v31, v4, v31
	v_add_f32_e32 v4, v4, v7
	v_fma_f32 v7, v5, s41, -v32
	v_add_f32_e32 v33, v27, v31
	v_add_f32_e32 v34, v29, v4
	v_fmac_f32_e32 v7, 0xb102e308, v5
	v_sub_f32_e32 v5, v33, v27
	v_sub_f32_e32 v27, v34, v29
	v_rcp_f32_e32 v29, v34
	v_add_f32_e32 v35, v32, v7
	v_sub_f32_e32 v4, v4, v27
	v_sub_f32_e32 v27, v35, v32
	v_sub_f32_e32 v7, v7, v27
	v_mul_f32_e32 v27, v33, v29
	v_sub_f32_e32 v5, v31, v5
	v_mul_f32_e32 v31, v34, v27
	v_fma_f32 v32, v27, v34, -v31
	v_fmac_f32_e32 v32, v27, v4
	v_add_f32_e32 v36, v31, v32
	v_sub_f32_e32 v37, v33, v36
	v_sub_f32_e32 v31, v36, v31
	v_sub_f32_e32 v33, v33, v37
	v_sub_f32_e32 v31, v31, v32
	v_sub_f32_e32 v32, v33, v36
	v_add_f32_e32 v5, v5, v32
	v_add_f32_e32 v5, v31, v5
	v_add_f32_e32 v31, v37, v5
	v_mul_f32_e32 v32, v29, v31
	v_sub_f32_e32 v33, v37, v31
	v_mul_f32_e32 v36, v34, v32
	v_add_f32_e32 v5, v5, v33
	v_add_f32_e32 v33, v27, v32
	v_fma_f32 v34, v32, v34, -v36
	v_sub_f32_e32 v27, v33, v27
	v_fmac_f32_e32 v34, v32, v4
	v_sub_f32_e32 v4, v32, v27
	v_add_f32_e32 v27, v36, v34
	v_sub_f32_e32 v32, v27, v36
	v_sub_f32_e32 v36, v31, v27
	v_sub_f32_e32 v31, v31, v36
	v_sub_f32_e32 v27, v31, v27
	v_sub_f32_e32 v32, v32, v34
	v_add_f32_e32 v5, v5, v27
	v_add_f32_e32 v5, v32, v5
	v_add_f32_e32 v5, v36, v5
	v_mul_f32_e32 v5, v29, v5
	v_add_f32_e32 v4, v4, v5
	v_add_f32_e32 v5, v33, v4
	v_mul_f32_e32 v27, v5, v5
	v_fmamk_f32 v32, v27, 0x3e9b6dac, v15
	v_sub_f32_e32 v29, v5, v33
	v_ldexp_f32 v31, v5, 1
	v_mul_f32_e32 v5, v5, v27
	v_fmaak_f32 v27, v27, v32, 0x3f2aaada
	v_mul_f32_e32 v5, v5, v27
	v_add_f32_e32 v27, v31, v5
	v_sub_f32_e32 v4, v4, v29
	v_sub_f32_e32 v29, v27, v31
	v_ldexp_f32 v4, v4, 1
	v_sub_f32_e32 v5, v5, v29
	v_add_f32_e32 v4, v4, v5
	v_add_f32_e32 v5, v27, v4
	v_sub_f32_e32 v27, v5, v27
	v_add_f32_e32 v29, v35, v5
	v_sub_f32_e32 v4, v4, v27
	v_sub_f32_e32 v27, v29, v35
	v_sub_f32_e32 v31, v29, v27
	v_sub_f32_e32 v5, v5, v27
	v_add_f32_e32 v27, v7, v4
	v_sub_f32_e32 v31, v35, v31
	v_sub_f32_e32 v32, v27, v7
	v_add_f32_e32 v5, v5, v31
	v_sub_f32_e32 v31, v27, v32
	v_sub_f32_e32 v4, v4, v32
	v_sub_f32_e32 v7, v7, v31
	v_add_f32_e32 v5, v27, v5
	v_add_f32_e32 v4, v4, v7
	v_add_f32_e32 v7, v29, v5
	v_sub_f32_e32 v27, v7, v29
	v_sub_f32_e32 v5, v5, v27
	v_add_f32_e32 v4, v4, v5
	v_add_f32_e32 v4, v7, v4
	v_cmp_neq_f32_e32 vcc, s42, v20
	v_add_f32_e32 v26, -1.0, v25
	v_add_f32_e32 v30, 1.0, v26
	v_cndmask_b32_e32 v4, v16, v4, vcc
	v_cmp_ngt_f32_e32 vcc, -1.0, v20
	v_sub_f32_e32 v5, v25, v30
	v_add_f32_e32 v5, v6, v5
	v_cndmask_b32_e32 v4, v17, v4, vcc
	v_cmp_neq_f32_e32 vcc, -1.0, v20
	v_add_f32_e32 v7, v26, v5
	s_nop 0
	v_cndmask_b32_e32 v4, v18, v4, vcc
	v_cmp_lt_f32_e64 vcc, |v20|, s43
	s_nop 1
	v_cndmask_b32_e32 v4, v4, v20, vcc
	v_sub_f32_e32 v4, v24, v4
	v_add_f32_e32 v24, 1.0, v25
	v_sub_f32_e32 v20, v7, v26
	v_add_f32_e32 v26, -1.0, v24
	v_sub_f32_e32 v25, v25, v26
	v_add_f32_e32 v6, v6, v25
	v_add_f32_e32 v25, v24, v6
	v_rcp_f32_e32 v26, v25
	v_sub_f32_e32 v5, v5, v20
	v_sub_f32_e32 v20, v25, v24
	v_sub_f32_e32 v6, v6, v20
	v_mul_f32_e32 v20, v7, v26
	v_mul_f32_e32 v24, v25, v20
	v_fma_f32 v27, v20, v25, -v24
	v_fmac_f32_e32 v27, v20, v6
	v_add_f32_e32 v29, v24, v27
	v_sub_f32_e32 v30, v7, v29
	v_sub_f32_e32 v7, v7, v30
	v_sub_f32_e32 v24, v29, v24
	v_sub_f32_e32 v7, v7, v29
	v_add_f32_e32 v5, v5, v7
	v_sub_f32_e32 v7, v24, v27
	v_add_f32_e32 v5, v7, v5
	v_add_f32_e32 v7, v30, v5
	v_mul_f32_e32 v24, v26, v7
	v_mul_f32_e32 v27, v25, v24
	v_fma_f32 v25, v24, v25, -v27
	v_fmac_f32_e32 v25, v24, v6
	v_sub_f32_e32 v6, v30, v7
	v_add_f32_e32 v5, v5, v6
	v_add_f32_e32 v6, v27, v25
	v_sub_f32_e32 v29, v7, v6
	v_sub_f32_e32 v7, v7, v29
	v_sub_f32_e32 v27, v6, v27
	v_sub_f32_e32 v6, v7, v6
	v_add_f32_e32 v5, v5, v6
	v_sub_f32_e32 v6, v27, v25
	v_add_f32_e32 v5, v6, v5
	v_add_f32_e32 v6, v20, v24
	v_sub_f32_e32 v7, v6, v20
	v_cvt_f32_i32_e32 v20, v28
	v_add_f32_e32 v5, v29, v5
	v_mul_f32_e32 v5, v26, v5
	v_sub_f32_e32 v7, v24, v7
	v_add_f32_e32 v5, v7, v5
	v_mul_f32_e32 v26, 0x3f317218, v20
	v_add_f32_e32 v7, v6, v5
	v_fma_f32 v27, v20, s41, -v26
	v_mul_f32_e32 v24, v7, v7
	v_fmac_f32_e32 v27, 0xb102e308, v20
	v_sub_f32_e32 v6, v7, v6
	v_fmamk_f32 v25, v24, 0x3e9b6dac, v15
	v_sub_f32_e32 v5, v5, v6
	v_add_f32_e32 v6, v26, v27
	v_fmaak_f32 v25, v24, v25, 0x3f2aaada
	v_sub_f32_e32 v20, v6, v26
	v_ldexp_f32 v26, v7, 1
	v_mul_f32_e32 v7, v7, v24
	v_mul_f32_e32 v7, v7, v25
	v_add_f32_e32 v24, v26, v7
	v_sub_f32_e32 v25, v24, v26
	v_ldexp_f32 v5, v5, 1
	v_sub_f32_e32 v7, v7, v25
	v_add_f32_e32 v5, v5, v7
	v_add_f32_e32 v7, v24, v5
	v_sub_f32_e32 v24, v7, v24
	v_sub_f32_e32 v5, v5, v24
	v_add_f32_e32 v24, v6, v7
	v_sub_f32_e32 v25, v24, v6
	v_sub_f32_e32 v26, v24, v25
	v_sub_f32_e32 v20, v27, v20
	v_sub_f32_e32 v6, v6, v26
	v_sub_f32_e32 v7, v7, v25
	v_add_f32_e32 v6, v7, v6
	v_add_f32_e32 v7, v20, v5
	v_sub_f32_e32 v25, v7, v20
	v_sub_f32_e32 v26, v7, v25
	v_add_f32_e32 v6, v7, v6
	v_sub_f32_e32 v20, v20, v26
	v_sub_f32_e32 v5, v5, v25
	v_add_f32_e32 v7, v24, v6
	v_add_f32_e32 v5, v5, v20
	v_sub_f32_e32 v20, v7, v24
	v_sub_f32_e32 v6, v6, v20
	v_add_f32_e32 v5, v5, v6
	s_waitcnt vmcnt(1)
	v_add_f32_e32 v6, v8, v21
	v_add_f32_e32 v5, v7, v5
	v_mul_f32_e64 v7, |v6|, s3
	v_exp_f32_e32 v20, v7
	v_cmp_neq_f32_e32 vcc, s42, v19
	v_add_f32_e32 v21, 1.0, v20
	s_nop 0
	v_cndmask_b32_e32 v5, v16, v5, vcc
	v_cmp_ngt_f32_e32 vcc, -1.0, v19
	v_frexp_mant_f32_e32 v24, v21
	s_nop 0
	v_cndmask_b32_e32 v5, v17, v5, vcc
	v_cmp_neq_f32_e32 vcc, -1.0, v19
	s_nop 1
	v_cndmask_b32_e32 v5, v18, v5, vcc
	v_cmp_lt_f32_e64 vcc, |v19|, s43
	s_nop 1
	v_cndmask_b32_e32 v5, v5, v19, vcc
	v_min_f32_e32 v19, 0, v6
	v_add_f32_e32 v6, -1.0, v21
	v_sub_f32_e32 v7, v6, v21
	v_add_f32_e32 v7, 1.0, v7
	v_sub_f32_e32 v6, v20, v6
	v_sub_f32_e32 v5, v23, v5
	v_add_f32_e32 v23, v6, v7
	v_cvt_f64_f32_e32 v[6:7], v21
	v_frexp_exp_i32_f64_e32 v6, v[6:7]
	v_cmp_gt_f32_e32 vcc, s40, v24
	v_add_f32_e32 v5, v4, v5
	s_nop 0
	v_subbrev_co_u32_e32 v6, vcc, 0, v6, vcc
	v_sub_u32_e32 v7, 0, v6
	v_ldexp_f32 v21, v21, v7
	v_ldexp_f32 v7, v23, v7
	v_add_f32_e32 v23, -1.0, v21
	v_add_f32_e32 v26, 1.0, v21
	v_add_f32_e32 v24, 1.0, v23
	v_add_f32_e32 v27, -1.0, v26
	v_sub_f32_e32 v24, v21, v24
	v_sub_f32_e32 v21, v21, v27
	v_add_f32_e32 v24, v7, v24
	v_add_f32_e32 v7, v7, v21
	v_add_f32_e32 v21, v26, v7
	v_rcp_f32_e32 v27, v21
	v_add_f32_e32 v25, v23, v24
	v_sub_f32_e32 v23, v25, v23
	v_sub_f32_e32 v23, v24, v23
	v_sub_f32_e32 v24, v21, v26
	v_sub_f32_e32 v7, v7, v24
	v_mul_f32_e32 v24, v25, v27
	v_mul_f32_e32 v26, v21, v24
	v_fma_f32 v28, v24, v21, -v26
	v_fmac_f32_e32 v28, v24, v7
	v_add_f32_e32 v29, v26, v28
	v_sub_f32_e32 v30, v25, v29
	v_sub_f32_e32 v25, v25, v30
	v_sub_f32_e32 v26, v29, v26
	v_sub_f32_e32 v25, v25, v29
	v_add_f32_e32 v23, v23, v25
	v_sub_f32_e32 v25, v26, v28
	v_add_f32_e32 v23, v25, v23
	v_add_f32_e32 v25, v30, v23
	v_mul_f32_e32 v26, v27, v25
	v_mul_f32_e32 v28, v21, v26
	v_fma_f32 v21, v26, v21, -v28
	v_fmac_f32_e32 v21, v26, v7
	v_sub_f32_e32 v7, v30, v25
	v_add_f32_e32 v7, v23, v7
	v_add_f32_e32 v23, v28, v21
	v_sub_f32_e32 v29, v25, v23
	v_sub_f32_e32 v25, v25, v29
	v_sub_f32_e32 v28, v23, v28
	v_sub_f32_e32 v23, v25, v23
	v_add_f32_e32 v7, v7, v23
	v_sub_f32_e32 v21, v28, v21
	v_cvt_f32_i32_e32 v6, v6
	v_add_f32_e32 v7, v21, v7
	v_add_f32_e32 v21, v24, v26
	v_add_f32_e32 v7, v29, v7
	v_sub_f32_e32 v23, v21, v24
	v_mul_f32_e32 v7, v27, v7
	v_sub_f32_e32 v23, v26, v23
	v_add_f32_e32 v7, v23, v7
	v_mul_f32_e32 v26, 0x3f317218, v6
	v_add_f32_e32 v23, v21, v7
	v_fma_f32 v27, v6, s41, -v26
	v_mul_f32_e32 v24, v23, v23
	v_fmac_f32_e32 v27, 0xb102e308, v6
	v_sub_f32_e32 v6, v23, v21
	v_fmamk_f32 v25, v24, 0x3e9b6dac, v15
	v_sub_f32_e32 v6, v7, v6
	v_add_f32_e32 v7, v26, v27
	v_fmaak_f32 v25, v24, v25, 0x3f2aaada
	v_sub_f32_e32 v21, v7, v26
	v_ldexp_f32 v26, v23, 1
	v_mul_f32_e32 v23, v23, v24
	v_mul_f32_e32 v23, v23, v25
	v_add_f32_e32 v24, v26, v23
	v_sub_f32_e32 v25, v24, v26
	v_ldexp_f32 v6, v6, 1
	v_sub_f32_e32 v23, v23, v25
	v_add_f32_e32 v6, v6, v23
	v_add_f32_e32 v23, v24, v6
	v_sub_f32_e32 v24, v23, v24
	v_sub_f32_e32 v6, v6, v24
	v_add_f32_e32 v24, v7, v23
	v_sub_f32_e32 v25, v24, v7
	v_sub_f32_e32 v26, v24, v25
	v_sub_f32_e32 v21, v27, v21
	v_sub_f32_e32 v7, v7, v26
	v_sub_f32_e32 v23, v23, v25
	v_add_f32_e32 v7, v23, v7
	v_add_f32_e32 v23, v21, v6
	v_sub_f32_e32 v25, v23, v21
	v_sub_f32_e32 v26, v23, v25
	v_sub_f32_e32 v21, v21, v26
	v_sub_f32_e32 v6, v6, v25
	v_add_f32_e32 v7, v23, v7
	v_add_f32_e32 v6, v6, v21
	v_add_f32_e32 v21, v24, v7
	v_sub_f32_e32 v23, v21, v24
	v_sub_f32_e32 v7, v7, v23
	v_add_f32_e32 v6, v6, v7
	s_waitcnt vmcnt(0)
	v_add_f32_e32 v7, v8, v22
	v_mul_f32_e64 v8, |v7|, s3
	v_add_f32_e32 v6, v21, v6
	v_cmp_neq_f32_e32 vcc, s42, v20
	v_exp_f32_e32 v8, v8
	s_nop 0
	v_cndmask_b32_e32 v6, v16, v6, vcc
	v_cmp_ngt_f32_e32 vcc, -1.0, v20
	v_add_f32_e32 v21, 1.0, v8
	v_frexp_mant_f32_e32 v23, v21
	v_cndmask_b32_e32 v6, v17, v6, vcc
	v_cmp_neq_f32_e32 vcc, -1.0, v20
	s_nop 1
	v_cndmask_b32_e32 v6, v18, v6, vcc
	v_cmp_lt_f32_e64 vcc, |v20|, s43
	s_nop 1
	v_cndmask_b32_e32 v6, v6, v20, vcc
	v_sub_f32_e32 v19, v19, v6
	v_add_f32_e32 v6, -1.0, v21
	v_min_f32_e32 v20, 0, v7
	v_sub_f32_e32 v7, v6, v21
	v_add_f32_e32 v7, 1.0, v7
	v_sub_f32_e32 v6, v8, v6
	v_add_f32_e32 v22, v6, v7
	v_cvt_f64_f32_e32 v[6:7], v21
	v_frexp_exp_i32_f64_e32 v6, v[6:7]
	v_cmp_gt_f32_e32 vcc, s40, v23
	s_nop 1
	v_subbrev_co_u32_e32 v6, vcc, 0, v6, vcc
	v_sub_u32_e32 v7, 0, v6
	v_ldexp_f32 v21, v21, v7
	v_ldexp_f32 v7, v22, v7
	v_add_f32_e32 v22, -1.0, v21
	v_add_f32_e32 v25, 1.0, v21
	v_add_f32_e32 v23, 1.0, v22
	v_add_f32_e32 v26, -1.0, v25
	v_sub_f32_e32 v23, v21, v23
	v_sub_f32_e32 v21, v21, v26
	v_add_f32_e32 v23, v7, v23
	v_add_f32_e32 v7, v7, v21
	v_add_f32_e32 v21, v25, v7
	v_rcp_f32_e32 v26, v21
	v_add_f32_e32 v24, v22, v23
	v_sub_f32_e32 v22, v24, v22
	v_sub_f32_e32 v22, v23, v22
	v_sub_f32_e32 v23, v21, v25
	v_sub_f32_e32 v7, v7, v23
	v_mul_f32_e32 v23, v24, v26
	v_mul_f32_e32 v25, v21, v23
	v_fma_f32 v27, v23, v21, -v25
	v_fmac_f32_e32 v27, v23, v7
	v_add_f32_e32 v28, v25, v27
	v_sub_f32_e32 v29, v24, v28
	v_sub_f32_e32 v24, v24, v29
	v_sub_f32_e32 v25, v28, v25
	v_sub_f32_e32 v24, v24, v28
	v_add_f32_e32 v22, v22, v24
	v_sub_f32_e32 v24, v25, v27
	v_add_f32_e32 v22, v24, v22
	v_add_f32_e32 v24, v29, v22
	v_mul_f32_e32 v25, v26, v24
	v_mul_f32_e32 v27, v21, v25
	v_fma_f32 v21, v25, v21, -v27
	v_fmac_f32_e32 v21, v25, v7
	v_sub_f32_e32 v7, v29, v24
	v_add_f32_e32 v7, v22, v7
	v_add_f32_e32 v22, v27, v21
	v_sub_f32_e32 v28, v24, v22
	v_sub_f32_e32 v24, v24, v28
	v_sub_f32_e32 v27, v22, v27
	v_sub_f32_e32 v22, v24, v22
	v_add_f32_e32 v7, v7, v22
	v_sub_f32_e32 v21, v27, v21
	v_cvt_f32_i32_e32 v6, v6
	v_add_f32_e32 v7, v21, v7
	v_add_f32_e32 v21, v23, v25
	v_add_f32_e32 v7, v28, v7
	v_sub_f32_e32 v22, v21, v23
	v_mul_f32_e32 v7, v26, v7
	v_sub_f32_e32 v22, v25, v22
	v_add_f32_e32 v7, v22, v7
	v_mul_f32_e32 v25, 0x3f317218, v6
	v_add_f32_e32 v22, v21, v7
	v_fma_f32 v26, v6, s41, -v25
	v_mul_f32_e32 v23, v22, v22
	v_fmac_f32_e32 v26, 0xb102e308, v6
	v_sub_f32_e32 v6, v22, v21
	v_fmamk_f32 v24, v23, 0x3e9b6dac, v15
	v_sub_f32_e32 v6, v7, v6
	v_add_f32_e32 v7, v25, v26
	v_fmaak_f32 v24, v23, v24, 0x3f2aaada
	v_sub_f32_e32 v21, v7, v25
	v_ldexp_f32 v25, v22, 1
	v_mul_f32_e32 v22, v22, v23
	v_mul_f32_e32 v22, v22, v24
	v_add_f32_e32 v23, v25, v22
	v_sub_f32_e32 v24, v23, v25
	v_ldexp_f32 v6, v6, 1
	v_sub_f32_e32 v22, v22, v24
	v_add_f32_e32 v6, v6, v22
	v_add_f32_e32 v22, v23, v6
	v_sub_f32_e32 v23, v22, v23
	v_sub_f32_e32 v6, v6, v23
	v_add_f32_e32 v23, v7, v22
	v_sub_f32_e32 v24, v23, v7
	v_sub_f32_e32 v25, v23, v24
	v_sub_f32_e32 v21, v26, v21
	v_sub_f32_e32 v7, v7, v25
	v_sub_f32_e32 v22, v22, v24
	v_add_f32_e32 v7, v22, v7
	v_add_f32_e32 v22, v21, v6
	v_sub_f32_e32 v24, v22, v21
	v_sub_f32_e32 v25, v22, v24
	v_sub_f32_e32 v21, v21, v25
	v_sub_f32_e32 v6, v6, v24
	v_add_f32_e32 v7, v22, v7
	v_add_f32_e32 v6, v6, v21
	v_add_f32_e32 v21, v23, v7
	v_sub_f32_e32 v22, v21, v23
	v_sub_f32_e32 v7, v7, v22
	v_add_f32_e32 v6, v6, v7
	v_add_f32_e32 v6, v21, v6
	v_cmp_neq_f32_e32 vcc, s42, v8
	s_nop 1
	v_cndmask_b32_e32 v6, v16, v6, vcc
	v_cmp_ngt_f32_e32 vcc, -1.0, v8
	s_nop 1
	v_cndmask_b32_e32 v6, v17, v6, vcc
	v_cmp_neq_f32_e32 vcc, -1.0, v8
	s_nop 1
	v_cndmask_b32_e32 v6, v18, v6, vcc
	v_cmp_lt_f32_e64 vcc, |v8|, s43
	s_nop 1
	v_cndmask_b32_e32 v6, v6, v8, vcc
	v_sub_f32_e32 v7, v20, v6
	v_add_f32_e32 v6, v5, v19
	v_add_f32_e32 v7, v6, v7
	ds_bpermute_b32 v8, v9, v7
	s_waitcnt lgkmcnt(0)
	v_add_f32_e32 v8, v7, v8
	v_cndmask_b32_e64 v8, v8, v7, s[8:9]
	ds_bpermute_b32 v19, v10, v8
	s_waitcnt lgkmcnt(0)
	v_add_f32_e32 v19, v8, v19
	v_cndmask_b32_e64 v8, v19, v8, s[10:11]
	ds_bpermute_b32 v19, v11, v8
	s_waitcnt lgkmcnt(0)
	v_add_f32_e32 v19, v8, v19
	v_cndmask_b32_e64 v8, v19, v8, s[12:13]
	ds_bpermute_b32 v19, v12, v8
	s_waitcnt lgkmcnt(0)
	v_add_f32_e32 v19, v8, v19
	v_cndmask_b32_e64 v8, v19, v8, s[14:15]
	ds_bpermute_b32 v19, v13, v8
	s_waitcnt lgkmcnt(0)
	v_add_f32_e32 v19, v8, v19
	v_cndmask_b32_e64 v19, v19, v8, s[16:17]
	ds_bpermute_b32 v8, v14, v19
	s_waitcnt lgkmcnt(0)
	v_add_f32_e32 v20, v19, v8
	s_and_saveexec_b64 s[34:35], s[4:5]
	ds_write_b32 v0, v20
	s_or_b64 exec, exec, s[34:35]
	v_mov_b32_e32 v8, 0
	s_waitcnt lgkmcnt(0)
	s_barrier
	s_and_saveexec_b64 s[34:35], s[6:7]
	s_cbranch_execz .LBB0_559
	v_mov_b32_e32 v8, 0
	s_and_saveexec_b64 s[36:37], s[20:21]
	s_cbranch_execz .LBB0_567
	s_mov_b32 s24, 0
	s_mov_b32 s31, 0
	s_mov_b64 s[38:39], 0
	v_mov_b32_e32 v8, 0
